# router partials stored/loaded write-through (sc0 sc1); the grid barrier between out-proj and router no longer writes back L2
# baseline (speedup 1.0000x reference)
; __device__ __forceinline__ unsigned cvt_pk_bf16(float lo, float hi) { unsigned r; asm volatile("v_cvt_pk_bf16_f32 %0, %1, %2" : "=v"(r) : "v"(lo), "v"(hi)); return r; }
; __device__ __forceinline__ unsigned pk4_fp8(float a, float b, float c, float d) { int p = 0; p = __builtin_amdgcn_cvt_pk_fp8_f32(a, b, p, false); p = __builtin_amdgcn_cvt_pk_fp8_f32(c, d, p, true); return (unsigned)p; }
;     __device__ __forceinline__ void operator()(AccRef acc, const Unit& u, int wr, int wc, int fr, int fq) const {
;     ...
; #pragma unroll
;         for (int ai = 0; ai < 2; ++ai)
; #pragma unroll
;             for (int m = 0; m < 4; ++m) { const size_t ro = (size_t)(row0 + ai * HALF + m * 16) * DM + col0;
;                 f32x4 xv[2][2];
; #pragma unroll
;                 for (int bj = 0; bj < 2; ++bj)
; #pragma unroll
;                     for (int n = 0; n < 2; ++n) xv[bj][n] = __builtin_nontemporal_load((const f32x4*)(X + ro + bj * HALF + 4 * n));
; #pragma unroll
;                 for (int bj = 0; bj < 2; ++bj) { const f32x4 a = xv[bj][0] + acc[ai][bj][m][0], b = xv[bj][1] + acc[ai][bj][m][1];
;                     { v4u xo; xo.x = cvt_pk_bf16(a[0], a[1]); xo.y = cvt_pk_bf16(a[2], a[3]); xo.z = cvt_pk_bf16(b[0], b[1]); xo.w = cvt_pk_bf16(b[2], b[3]); *(v4u*)(O + ro + bj * HALF) = xo; }
;                     const f32x4 ha = a * gv[bj][0], hb = b * gv[bj][1];
;                     v2u w; w.x = pk4_fp8(ha[0], ha[1], ha[2], ha[3]); w.y = pk4_fp8(hb[0], hb[1], hb[2], hb[3]);
;                     *(v2u*)((unsigned char*)HN + ro + bj * HALF) = w; } }
.LBB0_489:
	v_lshlrev_b32_e32 v241, 1, v254
	v_and_b32_e32 v252, 0x7ff, v254
	v_mbcnt_lo_u32_b32 v243, -1, 0
	v_mbcnt_hi_u32_b32 v243, -1, v243
	v_and_b32_e32 v243, 15, v243
	v_lshl_add_u32 v243, v243, 11, v252
	v_lshlrev_b32_e32 v243, 1, v243
	v_lshlrev_b32_e32 v252, 2, v252
	global_load_dwordx4 v[108:111], v252, s[10:11]
	global_load_dwordx4 v[104:107], v252, s[10:11] offset:16
	global_load_dwordx4 v[100:103], v252, s[10:11] offset:512
	global_load_dwordx4 v[96:99], v252, s[10:11] offset:528
	s_add_u32 s12, s36, 0x40000
	s_addc_u32 s13, s37, 0
	global_load_dwordx4 v[164:167], v240, s[12:13] nt
	global_load_dwordx4 v[168:171], v240, s[12:13] offset:16 nt
	global_load_dwordx4 v[172:175], v240, s[12:13] offset:512 nt
	global_load_dwordx4 v[176:179], v240, s[12:13] offset:528 nt
	s_add_u32 s12, s36, 0x60000
	s_addc_u32 s13, s37, 0
	global_load_dwordx4 v[180:183], v240, s[12:13] nt
	global_load_dwordx4 v[184:187], v240, s[12:13] offset:16 nt
	global_load_dwordx4 v[188:191], v240, s[12:13] offset:512 nt
	global_load_dwordx4 v[192:195], v240, s[12:13] offset:528 nt
	s_add_u32 s12, s36, 0x100000
	s_addc_u32 s13, s37, 0
	global_load_dwordx4 v[196:199], v240, s[12:13] nt
	global_load_dwordx4 v[200:203], v240, s[12:13] offset:16 nt
	global_load_dwordx4 v[204:207], v240, s[12:13] offset:512 nt
	global_load_dwordx4 v[148:151], v240, s[12:13] offset:528 nt
	s_nop 1
	s_waitcnt vmcnt(12)
	v_pk_add_f32 v[140:141], v[140:141], v[208:209]
	v_pk_add_f32 v[142:143], v[142:143], v[210:211]
	v_pk_add_f32 v[136:137], v[136:137], v[212:213]
	v_pk_add_f32 v[138:139], v[138:139], v[214:215]
	v_pk_add_f32 v[132:133], v[132:133], v[216:217]
	v_pk_add_f32 v[134:135], v[134:135], v[218:219]
	v_pk_add_f32 v[128:129], v[128:129], v[220:221]
	v_pk_add_f32 v[130:131], v[130:131], v[222:223]
	s_add_u32 s16, s38, 0x0
	s_addc_u32 s17, s39, 0
	s_add_u32 s20, s60, 0x0
	s_addc_u32 s21, s61, 0
	v_pk_mul_f32 v[208:209], v[108:109], v[140:141]
	v_pk_mul_f32 v[210:211], v[110:111], v[142:143]
	v_pk_mul_f32 v[212:213], v[104:105], v[136:137]
	v_pk_mul_f32 v[214:215], v[106:107], v[138:139]
	v_pk_mul_f32 v[216:217], v[100:101], v[132:133]
	v_pk_mul_f32 v[218:219], v[102:103], v[134:135]
	v_pk_mul_f32 v[220:221], v[96:97], v[128:129]
	v_pk_mul_f32 v[222:223], v[98:99], v[130:131]
	s_nop 0
	v_cvt_pk_bf16_f32 v140, v140, v141
	v_cvt_pk_bf16_f32 v141, v142, v143
	v_cvt_pk_bf16_f32 v142, v136, v137
	v_cvt_pk_bf16_f32 v143, v138, v139
	v_cvt_pk_bf16_f32 v132, v132, v133
	v_cvt_pk_bf16_f32 v133, v134, v135
	v_cvt_pk_bf16_f32 v134, v128, v129
	v_cvt_pk_bf16_f32 v135, v130, v131
	global_store_dwordx4 v241, v[140:143], s[16:17]
	global_store_dwordx4 v241, v[132:135], s[16:17] offset:256
	v_cvt_pk_fp8_f32 v252, v208, v209
	v_cvt_pk_fp8_f32 v253, v212, v213
	v_cvt_pk_fp8_f32 v242, v216, v217
	v_cvt_pk_fp8_f32 v243, v220, v221
	v_cvt_pk_fp8_f32 v252, v210, v211 op_sel:[0,0,1]
	v_cvt_pk_fp8_f32 v253, v214, v215 op_sel:[0,0,1]
	v_cvt_pk_fp8_f32 v242, v218, v219 op_sel:[0,0,1]
	v_cvt_pk_fp8_f32 v243, v222, v223 op_sel:[0,0,1]
	s_nop 0
	global_store_dwordx2 v254, v[252:253], s[20:21]
	global_store_dwordx2 v254, v[242:243], s[20:21] offset:128
	s_nop 1
	s_add_u32 s12, s36, 0x120000
	s_addc_u32 s13, s37, 0
	global_load_dwordx4 v[208:211], v240, s[12:13] nt
	global_load_dwordx4 v[212:215], v240, s[12:13] offset:16 nt
	global_load_dwordx4 v[216:219], v240, s[12:13] offset:512 nt
	global_load_dwordx4 v[220:223], v240, s[12:13] offset:528 nt
	v_pk_add_f32 v[124:125], v[124:125], v[224:225]
	v_pk_add_f32 v[126:127], v[126:127], v[226:227]
	v_pk_add_f32 v[120:121], v[120:121], v[228:229]
	v_pk_add_f32 v[122:123], v[122:123], v[230:231]
	v_pk_add_f32 v[116:117], v[116:117], v[232:233]
	v_pk_add_f32 v[118:119], v[118:119], v[234:235]
	v_pk_add_f32 v[112:113], v[112:113], v[236:237]
	v_pk_add_f32 v[114:115], v[114:115], v[238:239]
	s_add_u32 s16, s38, 0x10000
	s_addc_u32 s17, s39, 0
	s_add_u32 s20, s60, 0x8000
	s_addc_u32 s21, s61, 0
	v_pk_mul_f32 v[224:225], v[108:109], v[124:125]
	v_pk_mul_f32 v[226:227], v[110:111], v[126:127]
	v_pk_mul_f32 v[228:229], v[104:105], v[120:121]
	v_pk_mul_f32 v[230:231], v[106:107], v[122:123]
	v_pk_mul_f32 v[232:233], v[100:101], v[116:117]
	v_pk_mul_f32 v[234:235], v[102:103], v[118:119]
	v_pk_mul_f32 v[236:237], v[96:97], v[112:113]
	v_pk_mul_f32 v[238:239], v[98:99], v[114:115]
	s_nop 0
	v_cvt_pk_bf16_f32 v124, v124, v125
	v_cvt_pk_bf16_f32 v125, v126, v127
	v_cvt_pk_bf16_f32 v126, v120, v121
	v_cvt_pk_bf16_f32 v127, v122, v123
	v_cvt_pk_bf16_f32 v116, v116, v117
	v_cvt_pk_bf16_f32 v117, v118, v119
	v_cvt_pk_bf16_f32 v118, v112, v113
	v_cvt_pk_bf16_f32 v119, v114, v115
	global_store_dwordx4 v241, v[124:127], s[16:17]
	global_store_dwordx4 v241, v[116:119], s[16:17] offset:256
	v_cvt_pk_fp8_f32 v252, v224, v225
	v_cvt_pk_fp8_f32 v253, v228, v229
	v_cvt_pk_fp8_f32 v242, v232, v233
	v_cvt_pk_fp8_f32 v243, v236, v237
	v_cvt_pk_fp8_f32 v252, v226, v227 op_sel:[0,0,1]
	v_cvt_pk_fp8_f32 v253, v230, v231 op_sel:[0,0,1]
	v_cvt_pk_fp8_f32 v242, v234, v235 op_sel:[0,0,1]
	v_cvt_pk_fp8_f32 v243, v238, v239 op_sel:[0,0,1]
	s_nop 0
	global_store_dwordx2 v254, v[252:253], s[20:21]
	global_store_dwordx2 v254, v[242:243], s[20:21] offset:128
	s_nop 1
	s_add_u32 s12, s36, 0x140000
	s_addc_u32 s13, s37, 0
	global_load_dwordx4 v[224:227], v240, s[12:13] nt
	global_load_dwordx4 v[228:231], v240, s[12:13] offset:16 nt
	global_load_dwordx4 v[232:235], v240, s[12:13] offset:512 nt
	global_load_dwordx4 v[236:239], v240, s[12:13] offset:528 nt
	s_waitcnt vmcnt(24)
; __device__ __forceinline__ unsigned cvt_pk_bf16(float lo, float hi) { unsigned r; asm volatile("v_cvt_pk_bf16_f32 %0, %1, %2" : "=v"(r) : "v"(lo), "v"(hi)); return r; }
; __device__ __forceinline__ unsigned pk4_fp8(float a, float b, float c, float d) { int p = 0; p = __builtin_amdgcn_cvt_pk_fp8_f32(a, b, p, false); p = __builtin_amdgcn_cvt_pk_fp8_f32(c, d, p, true); return (unsigned)p; }
;     __device__ __forceinline__ void operator()(AccRef acc, const Unit& u, int wr, int wc, int fr, int fq) const {
;     ...
;             for (int m = 0; m < 4; ++m) { const size_t ro = (size_t)(row0 + ai * HALF + m * 16) * DM + col0;
;                 f32x4 xv[2][2];
; #pragma unroll
;                 for (int bj = 0; bj < 2; ++bj)
; #pragma unroll
;                     for (int n = 0; n < 2; ++n) xv[bj][n] = __builtin_nontemporal_load((const f32x4*)(X + ro + bj * HALF + 4 * n));
; #pragma unroll
;                 for (int bj = 0; bj < 2; ++bj) { const f32x4 a = xv[bj][0] + acc[ai][bj][m][0], b = xv[bj][1] + acc[ai][bj][m][1];
;                     { v4u xo; xo.x = cvt_pk_bf16(a[0], a[1]); xo.y = cvt_pk_bf16(a[2], a[3]); xo.z = cvt_pk_bf16(b[0], b[1]); xo.w = cvt_pk_bf16(b[2], b[3]); *(v4u*)(O + ro + bj * HALF) = xo; }
;                     const f32x4 ha = a * gv[bj][0], hb = b * gv[bj][1];
;                     v2u w; w.x = pk4_fp8(ha[0], ha[1], ha[2], ha[3]); w.y = pk4_fp8(hb[0], hb[1], hb[2], hb[3]);
;                     *(v2u*)((unsigned char*)HN + ro + bj * HALF) = w; } }
; __global__ void __launch_bounds__(512, 2) hymba_fwd(Args args) {
;     ...
;                         for (int x = 0; x < 2; ++x) xa[x][s4] = *(const v4u*)(xp + (size_t)(16 * x) * DM + ko);
; #pragma unroll
;                         for (int nt = 0; nt < 3; ++nt) { bh[s4][nt] = *(const bf16x8*)(hp + (size_t)(16 * nt) * DM + ko); bl[s4][nt] = *(const bf16x8*)(lp + (size_t)(16 * nt) * DM + ko); } }
	v_pk_add_f32 v[92:93], v[92:93], v[164:165]
	v_pk_add_f32 v[94:95], v[94:95], v[166:167]
	v_pk_add_f32 v[88:89], v[88:89], v[168:169]
	v_pk_add_f32 v[90:91], v[90:91], v[170:171]
	v_pk_add_f32 v[84:85], v[84:85], v[172:173]
	v_pk_add_f32 v[86:87], v[86:87], v[174:175]
	v_pk_add_f32 v[80:81], v[80:81], v[176:177]
	v_pk_add_f32 v[82:83], v[82:83], v[178:179]
	s_add_u32 s16, s38, 0x20000
	s_addc_u32 s17, s39, 0
	s_add_u32 s20, s60, 0x10000
	s_addc_u32 s21, s61, 0
	v_pk_mul_f32 v[164:165], v[108:109], v[92:93]
	v_pk_mul_f32 v[166:167], v[110:111], v[94:95]
	v_pk_mul_f32 v[168:169], v[104:105], v[88:89]
	v_pk_mul_f32 v[170:171], v[106:107], v[90:91]
	v_pk_mul_f32 v[172:173], v[100:101], v[84:85]
	v_pk_mul_f32 v[174:175], v[102:103], v[86:87]
	v_pk_mul_f32 v[176:177], v[96:97], v[80:81]
	v_pk_mul_f32 v[178:179], v[98:99], v[82:83]
	s_nop 0
	v_cvt_pk_bf16_f32 v92, v92, v93
	v_cvt_pk_bf16_f32 v93, v94, v95
	v_cvt_pk_bf16_f32 v94, v88, v89
	v_cvt_pk_bf16_f32 v95, v90, v91
	v_cvt_pk_bf16_f32 v84, v84, v85
	v_cvt_pk_bf16_f32 v85, v86, v87
	v_cvt_pk_bf16_f32 v86, v80, v81
	v_cvt_pk_bf16_f32 v87, v82, v83
	global_store_dwordx4 v241, v[92:95], s[16:17]
	global_store_dwordx4 v241, v[84:87], s[16:17] offset:256
	v_cvt_pk_fp8_f32 v252, v164, v165
	v_cvt_pk_fp8_f32 v253, v168, v169
	v_cvt_pk_fp8_f32 v242, v172, v173
	v_cvt_pk_fp8_f32 v243, v176, v177
	v_cvt_pk_fp8_f32 v252, v166, v167 op_sel:[0,0,1]
	v_cvt_pk_fp8_f32 v253, v170, v171 op_sel:[0,0,1]
	v_cvt_pk_fp8_f32 v242, v174, v175 op_sel:[0,0,1]
	v_cvt_pk_fp8_f32 v243, v178, v179 op_sel:[0,0,1]
	s_nop 0
	global_store_dwordx2 v254, v[252:253], s[20:21]
	global_store_dwordx2 v254, v[242:243], s[20:21] offset:128
	s_nop 1
	s_add_u32 s12, s36, 0x160000
	s_addc_u32 s13, s37, 0
	global_load_dwordx4 v[164:167], v240, s[12:13] nt
	global_load_dwordx4 v[168:171], v240, s[12:13] offset:16 nt
	global_load_dwordx4 v[172:175], v240, s[12:13] offset:512 nt
	global_load_dwordx4 v[176:179], v240, s[12:13] offset:528 nt
	s_waitcnt vmcnt(28)
	v_pk_add_f32 v[76:77], v[76:77], v[180:181]
	v_pk_add_f32 v[78:79], v[78:79], v[182:183]
	v_pk_add_f32 v[72:73], v[72:73], v[184:185]
	v_pk_add_f32 v[74:75], v[74:75], v[186:187]
	v_pk_add_f32 v[68:69], v[68:69], v[188:189]
	v_pk_add_f32 v[70:71], v[70:71], v[190:191]
	v_pk_add_f32 v[64:65], v[64:65], v[192:193]
	v_pk_add_f32 v[66:67], v[66:67], v[194:195]
	s_add_u32 s16, s38, 0x30000
	s_addc_u32 s17, s39, 0
	s_add_u32 s20, s60, 0x18000
	s_addc_u32 s21, s61, 0
	v_pk_mul_f32 v[180:181], v[108:109], v[76:77]
	v_pk_mul_f32 v[182:183], v[110:111], v[78:79]
	v_pk_mul_f32 v[184:185], v[104:105], v[72:73]
	v_pk_mul_f32 v[186:187], v[106:107], v[74:75]
	v_pk_mul_f32 v[188:189], v[100:101], v[68:69]
	v_pk_mul_f32 v[190:191], v[102:103], v[70:71]
	v_pk_mul_f32 v[192:193], v[96:97], v[64:65]
	v_pk_mul_f32 v[194:195], v[98:99], v[66:67]
	s_nop 0
	v_cvt_pk_bf16_f32 v76, v76, v77
	v_cvt_pk_bf16_f32 v77, v78, v79
	v_cvt_pk_bf16_f32 v78, v72, v73
	v_cvt_pk_bf16_f32 v79, v74, v75
	v_cvt_pk_bf16_f32 v68, v68, v69
	v_cvt_pk_bf16_f32 v69, v70, v71
	v_cvt_pk_bf16_f32 v70, v64, v65
	v_cvt_pk_bf16_f32 v71, v66, v67
	global_store_dwordx4 v241, v[76:79], s[16:17]
	global_store_dwordx4 v241, v[68:71], s[16:17] offset:256
	v_cvt_pk_fp8_f32 v252, v180, v181
	v_cvt_pk_fp8_f32 v253, v184, v185
	v_cvt_pk_fp8_f32 v242, v188, v189
	v_cvt_pk_fp8_f32 v243, v192, v193
	v_cvt_pk_fp8_f32 v252, v182, v183 op_sel:[0,0,1]
	v_cvt_pk_fp8_f32 v253, v186, v187 op_sel:[0,0,1]
	v_cvt_pk_fp8_f32 v242, v190, v191 op_sel:[0,0,1]
	v_cvt_pk_fp8_f32 v243, v194, v195 op_sel:[0,0,1]
	s_nop 0
	global_store_dwordx2 v254, v[252:253], s[20:21]
	global_store_dwordx2 v254, v[242:243], s[20:21] offset:128
	v_and_b32_e32 v244, 0x7ff, v254
	v_mbcnt_lo_u32_b32 v243, -1, 0
	v_mbcnt_hi_u32_b32 v243, -1, v243
	v_and_b32_e32 v243, 15, v243
	v_lshl_add_u32 v243, v243, 11, v244
	v_lshlrev_b32_e32 v243, 1, v243
	s_nop 1
	s_add_u32 s12, s26, 0x350000
	s_addc_u32 s13, s27, 0
	global_load_dwordx4 v[180:183], v243, s[12:13]
	s_add_u32 s12, s26, 0x320000
	s_addc_u32 s13, s27, 0
	global_load_dwordx4 v[184:187], v243, s[12:13]
	s_add_u32 s12, s26, 0x360000
	s_addc_u32 s13, s27, 0
	global_load_dwordx4 v[188:191], v243, s[12:13]
	s_add_u32 s12, s26, 0x330000
	s_addc_u32 s13, s27, 0
	global_load_dwordx4 v[192:195], v243, s[12:13]
	s_waitcnt vmcnt(32)
	v_pk_add_f32 v[60:61], v[60:61], v[196:197]
	v_pk_add_f32 v[62:63], v[62:63], v[198:199]
	v_pk_add_f32 v[56:57], v[56:57], v[200:201]
	v_pk_add_f32 v[58:59], v[58:59], v[202:203]
	v_pk_add_f32 v[52:53], v[52:53], v[204:205]
	v_pk_add_f32 v[54:55], v[54:55], v[206:207]
	v_pk_add_f32 v[48:49], v[48:49], v[148:149]
	v_pk_add_f32 v[50:51], v[50:51], v[150:151]
	s_add_u32 s16, s38, 0x80000
	s_addc_u32 s17, s39, 0
	s_add_u32 s20, s60, 0x40000
	s_addc_u32 s21, s61, 0
	v_pk_mul_f32 v[196:197], v[108:109], v[60:61]
	v_pk_mul_f32 v[198:199], v[110:111], v[62:63]
	v_pk_mul_f32 v[200:201], v[104:105], v[56:57]
	v_pk_mul_f32 v[202:203], v[106:107], v[58:59]
	v_pk_mul_f32 v[204:205], v[100:101], v[52:53]
	v_pk_mul_f32 v[206:207], v[102:103], v[54:55]
	v_pk_mul_f32 v[148:149], v[96:97], v[48:49]
	v_pk_mul_f32 v[150:151], v[98:99], v[50:51]
	s_nop 0
	v_cvt_pk_bf16_f32 v60, v60, v61
	v_cvt_pk_bf16_f32 v61, v62, v63
	v_cvt_pk_bf16_f32 v62, v56, v57
	v_cvt_pk_bf16_f32 v63, v58, v59
	v_cvt_pk_bf16_f32 v52, v52, v53
	v_cvt_pk_bf16_f32 v53, v54, v55
	v_cvt_pk_bf16_f32 v54, v48, v49
	v_cvt_pk_bf16_f32 v55, v50, v51
	global_store_dwordx4 v241, v[60:63], s[16:17]
	global_store_dwordx4 v241, v[52:55], s[16:17] offset:256
	v_cvt_pk_fp8_f32 v252, v196, v197
	v_cvt_pk_fp8_f32 v253, v200, v201
	v_cvt_pk_fp8_f32 v242, v204, v205
	v_cvt_pk_fp8_f32 v243, v148, v149
	v_cvt_pk_fp8_f32 v252, v198, v199 op_sel:[0,0,1]
	v_cvt_pk_fp8_f32 v253, v202, v203 op_sel:[0,0,1]
	v_cvt_pk_fp8_f32 v242, v206, v207 op_sel:[0,0,1]
	v_cvt_pk_fp8_f32 v243, v150, v151 op_sel:[0,0,1]
	s_nop 0
	global_store_dwordx2 v254, v[252:253], s[20:21]
	global_store_dwordx2 v254, v[242:243], s[20:21] offset:128
	v_and_b32_e32 v244, 0x7ff, v254
	v_mbcnt_lo_u32_b32 v243, -1, 0
	v_mbcnt_hi_u32_b32 v243, -1, v243
	v_and_b32_e32 v243, 15, v243
	v_lshl_add_u32 v243, v243, 11, v244
	v_lshlrev_b32_e32 v243, 1, v243
	s_nop 1
	s_add_u32 s12, s26, 0x370000
	s_addc_u32 s13, s27, 0
	global_load_dwordx4 v[196:199], v243, s[12:13]
	s_add_u32 s12, s26, 0x340000
	s_addc_u32 s13, s27, 0
	global_load_dwordx4 v[200:203], v243, s[12:13]
	s_add_u32 s12, s26, 0x350100
	s_addc_u32 s13, s27, 0
	global_load_dwordx4 v[204:207], v243, s[12:13]
	s_add_u32 s12, s26, 0x320100
	s_addc_u32 s13, s27, 0
	global_load_dwordx4 v[148:151], v243, s[12:13]
	s_waitcnt vmcnt(32)
; __device__ __forceinline__ unsigned cvt_pk_bf16(float lo, float hi) { unsigned r; asm volatile("v_cvt_pk_bf16_f32 %0, %1, %2" : "=v"(r) : "v"(lo), "v"(hi)); return r; }
; __device__ __forceinline__ unsigned pk4_fp8(float a, float b, float c, float d) { int p = 0; p = __builtin_amdgcn_cvt_pk_fp8_f32(a, b, p, false); p = __builtin_amdgcn_cvt_pk_fp8_f32(c, d, p, true); return (unsigned)p; }
;     __device__ __forceinline__ void operator()(AccRef acc, const Unit& u, int wr, int wc, int fr, int fq) const {
;     ...
;             for (int m = 0; m < 4; ++m) { const size_t ro = (size_t)(row0 + ai * HALF + m * 16) * DM + col0;
;                 f32x4 xv[2][2];
; #pragma unroll
;                 for (int bj = 0; bj < 2; ++bj)
; #pragma unroll
;                     for (int n = 0; n < 2; ++n) xv[bj][n] = __builtin_nontemporal_load((const f32x4*)(X + ro + bj * HALF + 4 * n));
; #pragma unroll
;                 for (int bj = 0; bj < 2; ++bj) { const f32x4 a = xv[bj][0] + acc[ai][bj][m][0], b = xv[bj][1] + acc[ai][bj][m][1];
;                     { v4u xo; xo.x = cvt_pk_bf16(a[0], a[1]); xo.y = cvt_pk_bf16(a[2], a[3]); xo.z = cvt_pk_bf16(b[0], b[1]); xo.w = cvt_pk_bf16(b[2], b[3]); *(v4u*)(O + ro + bj * HALF) = xo; }
;                     const f32x4 ha = a * gv[bj][0], hb = b * gv[bj][1];
;                     v2u w; w.x = pk4_fp8(ha[0], ha[1], ha[2], ha[3]); w.y = pk4_fp8(hb[0], hb[1], hb[2], hb[3]);
;                     *(v2u*)((unsigned char*)HN + ro + bj * HALF) = w; } }
; __global__ void __launch_bounds__(512, 2) hymba_fwd(Args args) {
;     ...
; #pragma unroll
;                 for (int x = 0; x < 2; ++x) {
; #pragma unroll
;                     for (int nt = 0; nt < 3; ++nt)
; #pragma unroll
;                         for (int e = 0; e < 4; ++e) part[(wave * 32 + 16 * x + 4 * kg + e) * 48 + 16 * nt + li] = acc[x][nt][e];
;                     float s1 = ss[x]; s1 += __shfl_xor(s1, 16); s1 += __shfl_xor(s1, 32);
;                     if (kg == 0) ssp[wave * 32 + 16 * x + li] = s1; }
	v_pk_add_f32 v[44:45], v[44:45], v[208:209]
	v_pk_add_f32 v[46:47], v[46:47], v[210:211]
	v_pk_add_f32 v[40:41], v[40:41], v[212:213]
	v_pk_add_f32 v[42:43], v[42:43], v[214:215]
	v_pk_add_f32 v[36:37], v[36:37], v[216:217]
	v_pk_add_f32 v[38:39], v[38:39], v[218:219]
	v_pk_add_f32 v[32:33], v[32:33], v[220:221]
	v_pk_add_f32 v[34:35], v[34:35], v[222:223]
	s_add_u32 s16, s38, 0x90000
	s_addc_u32 s17, s39, 0
	s_add_u32 s20, s60, 0x48000
	s_addc_u32 s21, s61, 0
	v_pk_mul_f32 v[208:209], v[108:109], v[44:45]
	v_pk_mul_f32 v[210:211], v[110:111], v[46:47]
	v_pk_mul_f32 v[212:213], v[104:105], v[40:41]
	v_pk_mul_f32 v[214:215], v[106:107], v[42:43]
	v_pk_mul_f32 v[216:217], v[100:101], v[36:37]
	v_pk_mul_f32 v[218:219], v[102:103], v[38:39]
	v_pk_mul_f32 v[220:221], v[96:97], v[32:33]
	v_pk_mul_f32 v[222:223], v[98:99], v[34:35]
	s_nop 0
	v_cvt_pk_bf16_f32 v44, v44, v45
	v_cvt_pk_bf16_f32 v45, v46, v47
	v_cvt_pk_bf16_f32 v46, v40, v41
	v_cvt_pk_bf16_f32 v47, v42, v43
	v_cvt_pk_bf16_f32 v36, v36, v37
	v_cvt_pk_bf16_f32 v37, v38, v39
	v_cvt_pk_bf16_f32 v38, v32, v33
	v_cvt_pk_bf16_f32 v39, v34, v35
	global_store_dwordx4 v241, v[44:47], s[16:17]
	global_store_dwordx4 v241, v[36:39], s[16:17] offset:256
	v_cvt_pk_fp8_f32 v252, v208, v209
	v_cvt_pk_fp8_f32 v253, v212, v213
	v_cvt_pk_fp8_f32 v242, v216, v217
	v_cvt_pk_fp8_f32 v243, v220, v221
	v_cvt_pk_fp8_f32 v252, v210, v211 op_sel:[0,0,1]
	v_cvt_pk_fp8_f32 v253, v214, v215 op_sel:[0,0,1]
	v_cvt_pk_fp8_f32 v242, v218, v219 op_sel:[0,0,1]
	v_cvt_pk_fp8_f32 v243, v222, v223 op_sel:[0,0,1]
	s_nop 0
	global_store_dwordx2 v254, v[252:253], s[20:21]
	global_store_dwordx2 v254, v[242:243], s[20:21] offset:128
	v_and_b32_e32 v244, 0x7ff, v254
	v_mbcnt_lo_u32_b32 v243, -1, 0
	v_mbcnt_hi_u32_b32 v243, -1, v243
	v_and_b32_e32 v243, 15, v243
	v_lshl_add_u32 v243, v243, 11, v244
	v_lshlrev_b32_e32 v243, 1, v243
	s_nop 1
	s_add_u32 s12, s26, 0x360100
	s_addc_u32 s13, s27, 0
	global_load_dwordx4 v[208:211], v243, s[12:13]
	s_add_u32 s12, s26, 0x330100
	s_addc_u32 s13, s27, 0
	global_load_dwordx4 v[212:215], v243, s[12:13]
	s_add_u32 s12, s26, 0x370100
	s_addc_u32 s13, s27, 0
	global_load_dwordx4 v[216:219], v243, s[12:13]
	s_add_u32 s12, s26, 0x340100
	s_addc_u32 s13, s27, 0
	global_load_dwordx4 v[220:223], v243, s[12:13]
	s_waitcnt vmcnt(32)
	v_pk_add_f32 v[20:21], v[20:21], v[224:225]
	v_pk_add_f32 v[22:23], v[22:23], v[226:227]
	v_pk_add_f32 v[16:17], v[16:17], v[228:229]
	v_pk_add_f32 v[18:19], v[18:19], v[230:231]
	v_pk_add_f32 v[24:25], v[24:25], v[232:233]
	v_pk_add_f32 v[26:27], v[26:27], v[234:235]
	v_pk_add_f32 v[28:29], v[28:29], v[236:237]
	v_pk_add_f32 v[30:31], v[30:31], v[238:239]
	s_add_u32 s16, s38, 0xa0000
	s_addc_u32 s17, s39, 0
	s_add_u32 s20, s60, 0x50000
	s_addc_u32 s21, s61, 0
	v_pk_mul_f32 v[224:225], v[108:109], v[20:21]
	v_pk_mul_f32 v[226:227], v[110:111], v[22:23]
	v_pk_mul_f32 v[228:229], v[104:105], v[16:17]
	v_pk_mul_f32 v[230:231], v[106:107], v[18:19]
	v_pk_mul_f32 v[232:233], v[100:101], v[24:25]
	v_pk_mul_f32 v[234:235], v[102:103], v[26:27]
	v_pk_mul_f32 v[236:237], v[96:97], v[28:29]
	v_pk_mul_f32 v[238:239], v[98:99], v[30:31]
	s_nop 0
	v_cvt_pk_bf16_f32 v20, v20, v21
	v_cvt_pk_bf16_f32 v21, v22, v23
	v_cvt_pk_bf16_f32 v22, v16, v17
	v_cvt_pk_bf16_f32 v23, v18, v19
	v_cvt_pk_bf16_f32 v24, v24, v25
	v_cvt_pk_bf16_f32 v25, v26, v27
	v_cvt_pk_bf16_f32 v26, v28, v29
	v_cvt_pk_bf16_f32 v27, v30, v31
	global_store_dwordx4 v241, v[20:23], s[16:17]
	global_store_dwordx4 v241, v[24:27], s[16:17] offset:256
	v_cvt_pk_fp8_f32 v252, v224, v225
	v_cvt_pk_fp8_f32 v253, v228, v229
	v_cvt_pk_fp8_f32 v242, v232, v233
	v_cvt_pk_fp8_f32 v243, v236, v237
	v_cvt_pk_fp8_f32 v252, v226, v227 op_sel:[0,0,1]
	v_cvt_pk_fp8_f32 v253, v230, v231 op_sel:[0,0,1]
	v_cvt_pk_fp8_f32 v242, v234, v235 op_sel:[0,0,1]
	v_cvt_pk_fp8_f32 v243, v238, v239 op_sel:[0,0,1]
	s_nop 0
	global_store_dwordx2 v254, v[252:253], s[20:21]
	global_store_dwordx2 v254, v[242:243], s[20:21] offset:128
	s_waitcnt vmcnt(28)
	v_pk_add_f32 v[4:5], v[4:5], v[164:165]
	v_pk_add_f32 v[6:7], v[6:7], v[166:167]
	v_pk_add_f32 v[0:1], v[0:1], v[168:169]
	v_pk_add_f32 v[2:3], v[2:3], v[170:171]
	v_pk_add_f32 v[8:9], v[8:9], v[172:173]
	v_pk_add_f32 v[10:11], v[10:11], v[174:175]
	v_pk_add_f32 v[12:13], v[12:13], v[176:177]
	v_pk_add_f32 v[14:15], v[14:15], v[178:179]
	s_add_u32 s16, s38, 0xb0000
	s_addc_u32 s17, s39, 0
	s_add_u32 s20, s60, 0x58000
	s_addc_u32 s21, s61, 0
	v_pk_mul_f32 v[164:165], v[108:109], v[4:5]
	v_pk_mul_f32 v[166:167], v[110:111], v[6:7]
	v_pk_mul_f32 v[168:169], v[104:105], v[0:1]
	v_pk_mul_f32 v[170:171], v[106:107], v[2:3]
	v_pk_mul_f32 v[172:173], v[100:101], v[8:9]
	v_pk_mul_f32 v[174:175], v[102:103], v[10:11]
	v_pk_mul_f32 v[176:177], v[96:97], v[12:13]
	v_pk_mul_f32 v[178:179], v[98:99], v[14:15]
	s_nop 0
	v_cvt_pk_bf16_f32 v4, v4, v5
	v_cvt_pk_bf16_f32 v5, v6, v7
	v_cvt_pk_bf16_f32 v6, v0, v1
	v_cvt_pk_bf16_f32 v7, v2, v3
	v_cvt_pk_bf16_f32 v8, v8, v9
	v_cvt_pk_bf16_f32 v9, v10, v11
	v_cvt_pk_bf16_f32 v10, v12, v13
	v_cvt_pk_bf16_f32 v11, v14, v15
	global_store_dwordx4 v241, v[4:7], s[16:17]
	global_store_dwordx4 v241, v[8:11], s[16:17] offset:256
	v_cvt_pk_fp8_f32 v252, v164, v165
	v_cvt_pk_fp8_f32 v253, v168, v169
	v_cvt_pk_fp8_f32 v242, v172, v173
	v_cvt_pk_fp8_f32 v243, v176, v177
	v_cvt_pk_fp8_f32 v252, v166, v167 op_sel:[0,0,1]
	v_cvt_pk_fp8_f32 v253, v170, v171 op_sel:[0,0,1]
	v_cvt_pk_fp8_f32 v242, v174, v175 op_sel:[0,0,1]
	v_cvt_pk_fp8_f32 v243, v178, v179 op_sel:[0,0,1]
	s_nop 0
	global_store_dwordx2 v254, v[252:253], s[20:21]
	global_store_dwordx2 v254, v[242:243], s[20:21] offset:128
	v_mbcnt_lo_u32_b32 v164, -1, 0
	v_mbcnt_hi_u32_b32 v164, -1, v164
	v_and_b32_e32 v165, 15, v164
	v_lshrrev_b32_e32 v166, 4, v164
	s_lshr_b32 s33, s77, 6
	s_lshr_b32 s41, s78, 5
	s_lshl_b32 s100, s33, 2
	s_add_i32 s100, s100, s41
	v_lshl_add_u32 v167, v166, 2, s77
	v_mul_u32_u24_e32 v167, 48, v167
	v_add_u32_e32 v167, v167, v165
	v_lshlrev_b32_e32 v167, 2, v167
	v_add_u32_e32 v168, s77, v165
	v_lshlrev_b32_e32 v168, 2, v168
	v_lshlrev_b32_e32 v169, 2, v166
	v_sub_u32_e32 v169, v165, v169
	v_cmp_eq_u32_e64 s[12:13], 0, v169
	v_cmp_eq_u32_e64 s[16:17], 1, v169
	v_cmp_eq_u32_e64 s[20:21], 2, v169
	v_cmp_eq_u32_e64 s[22:23], 3, v169
	s_barrier
; __global__ void __launch_bounds__(512, 2) hymba_fwd(Args args) {
;     ...
;                     for (int s4 = 0; s4 < 4; ++s4)
; #pragma unroll
;                         for (int x = 0; x < 2; ++x) { const bf16x8 xh = __builtin_bit_cast(bf16x8, xa[x][s4]);
; #pragma unroll
;                             for (int nt = 0; nt < 3; ++nt) {
;                                 acc[x][nt] = __builtin_amdgcn_mfma_f32_16x16x32_bf16(xh, bl[s4][nt], acc[x][nt], 0, 0, 0);
;                                 acc[x][nt] = __builtin_amdgcn_mfma_f32_16x16x32_bf16(xh, bh[s4][nt], acc[x][nt], 0, 0, 0); } }
;                 }
; #pragma unroll
;                 for (int x = 0; x < 2; ++x) {
; #pragma unroll
;                     for (int nt = 0; nt < 3; ++nt)
; #pragma unroll
;                         for (int e = 0; e < 4; ++e) part[(wave * 32 + 16 * x + 4 * kg + e) * 48 + 16 * nt + li] = acc[x][nt][e];
;                     float s1 = ss[x]; s1 += __shfl_xor(s1, 16); s1 += __shfl_xor(s1, 32);
;                     if (kg == 0) ssp[wave * 32 + 16 * x + li] = s1; }
	v_mov_b32_e32 v172, 0
	v_mov_b32_e32 v173, 0
	v_mov_b32_e32 v174, 0
	v_mov_b32_e32 v175, 0
	s_mul_i32 s101, s100, 0x1800
	v_lshl_add_u32 v170, v164, 4, s101
	ds_write_b128 v170, v[172:175] offset:0
	ds_write_b128 v170, v[172:175] offset:1024
	ds_write_b128 v170, v[172:175] offset:2048
	ds_write_b128 v170, v[172:175] offset:3072
	ds_write_b128 v170, v[172:175] offset:4096
	ds_write_b128 v170, v[172:175] offset:5120
	s_lshl_b32 s101, s100, 7
	v_lshl_add_u32 v171, v164, 2, s101
	s_mov_b32 exec_lo, -1
	s_mov_b32 exec_hi, 0
	ds_write_b32 v171, v172 offset:49152
	s_mov_b64 exec, -1
	s_waitcnt vmcnt(8) lgkmcnt(0)
	s_barrier
	v_mov_b32_e32 v176, 0x4b800000
	v_mov_b32_e32 v177, 0x47800000
	v_mfma_f32_16x16x32_bf16 v[224:227], v[140:143], v[180:183], 0
	v_mfma_f32_16x16x32_bf16 v[224:227], v[140:143], v[184:187], v[224:227]
	v_mfma_f32_16x16x32_bf16 v[224:227], v[132:135], v[204:207], v[224:227]
	v_mfma_f32_16x16x32_bf16 v[224:227], v[132:135], v[148:151], v[224:227]
	v_mfma_f32_16x16x32_bf16 v[228:231], v[140:143], v[188:191], 0
	v_mfma_f32_16x16x32_bf16 v[228:231], v[140:143], v[192:195], v[228:231]
	v_mfma_f32_16x16x32_bf16 v[228:231], v[132:135], v[208:211], v[228:231]
	v_mfma_f32_16x16x32_bf16 v[228:231], v[132:135], v[212:215], v[228:231]
	v_mfma_f32_16x16x32_bf16 v[232:235], v[140:143], v[196:199], 0
	v_mfma_f32_16x16x32_bf16 v[232:235], v[140:143], v[200:203], v[232:235]
	v_mfma_f32_16x16x32_bf16 v[232:235], v[132:135], v[216:219], v[232:235]
	v_mfma_f32_16x16x32_bf16 v[232:235], v[132:135], v[220:223], v[232:235]
	v_mfma_f32_16x16x32_bf16 v[236:239], v[140:143], v[140:143], 0
	v_mfma_f32_16x16x32_bf16 v[236:239], v[132:135], v[132:135], v[236:239]
	s_nop 7
	s_nop 3
	v_mul_f32_e32 v224, v224, v176
	v_cvt_i32_f32_e32 v224, v224
	v_mul_f32_e32 v225, v225, v176
	v_cvt_i32_f32_e32 v225, v225
	v_mul_f32_e32 v226, v226, v176
	v_cvt_i32_f32_e32 v226, v226
	v_mul_f32_e32 v227, v227, v176
	v_cvt_i32_f32_e32 v227, v227
	v_mul_f32_e32 v228, v228, v176
	v_cvt_i32_f32_e32 v228, v228
	v_mul_f32_e32 v229, v229, v176
	v_cvt_i32_f32_e32 v229, v229
	v_mul_f32_e32 v230, v230, v176
	v_cvt_i32_f32_e32 v230, v230
	v_mul_f32_e32 v231, v231, v176
	v_cvt_i32_f32_e32 v231, v231
	v_mul_f32_e32 v232, v232, v176
	v_cvt_i32_f32_e32 v232, v232
	v_mul_f32_e32 v233, v233, v176
	v_cvt_i32_f32_e32 v233, v233
	v_mul_f32_e32 v234, v234, v176
	v_cvt_i32_f32_e32 v234, v234
	v_mul_f32_e32 v235, v235, v176
	v_cvt_i32_f32_e32 v235, v235
	v_mul_f32_e32 v236, v236, v177
	v_cvt_i32_f32_e32 v236, v236
	v_mul_f32_e32 v237, v237, v177
	v_cvt_i32_f32_e32 v237, v237
	v_mul_f32_e32 v238, v238, v177
	v_cvt_i32_f32_e32 v238, v238
	v_mul_f32_e32 v239, v239, v177
	v_cvt_i32_f32_e32 v239, v239
	ds_add_u32 v167, v224 offset:0
	ds_add_u32 v167, v225 offset:192
	ds_add_u32 v167, v226 offset:384
	ds_add_u32 v167, v227 offset:576
	ds_add_u32 v167, v228 offset:64
	ds_add_u32 v167, v229 offset:256
	ds_add_u32 v167, v230 offset:448
	ds_add_u32 v167, v231 offset:640
	ds_add_u32 v167, v232 offset:128
	ds_add_u32 v167, v233 offset:320
	ds_add_u32 v167, v234 offset:512
	ds_add_u32 v167, v235 offset:704
	s_mov_b64 exec, s[12:13]
	ds_add_u32 v168, v236 offset:49152
	s_mov_b64 exec, s[16:17]
	ds_add_u32 v168, v237 offset:49152
	s_mov_b64 exec, s[20:21]
	ds_add_u32 v168, v238 offset:49152
	s_mov_b64 exec, s[22:23]
	ds_add_u32 v168, v239 offset:49152
	s_mov_b64 exec, -1
	v_mfma_f32_16x16x32_bf16 v[224:227], v[124:127], v[180:183], 0
	v_mfma_f32_16x16x32_bf16 v[224:227], v[124:127], v[184:187], v[224:227]
	v_mfma_f32_16x16x32_bf16 v[224:227], v[116:119], v[204:207], v[224:227]
	v_mfma_f32_16x16x32_bf16 v[224:227], v[116:119], v[148:151], v[224:227]
	v_mfma_f32_16x16x32_bf16 v[228:231], v[124:127], v[188:191], 0
	v_mfma_f32_16x16x32_bf16 v[228:231], v[124:127], v[192:195], v[228:231]
	v_mfma_f32_16x16x32_bf16 v[228:231], v[116:119], v[208:211], v[228:231]
	v_mfma_f32_16x16x32_bf16 v[228:231], v[116:119], v[212:215], v[228:231]
	v_mfma_f32_16x16x32_bf16 v[232:235], v[124:127], v[196:199], 0
	v_mfma_f32_16x16x32_bf16 v[232:235], v[124:127], v[200:203], v[232:235]
	v_mfma_f32_16x16x32_bf16 v[232:235], v[116:119], v[216:219], v[232:235]
	v_mfma_f32_16x16x32_bf16 v[232:235], v[116:119], v[220:223], v[232:235]
	v_mfma_f32_16x16x32_bf16 v[236:239], v[124:127], v[124:127], 0
	v_mfma_f32_16x16x32_bf16 v[236:239], v[116:119], v[116:119], v[236:239]
	s_nop 7
	s_nop 3
	v_mul_f32_e32 v224, v224, v176
	v_cvt_i32_f32_e32 v224, v224
	v_mul_f32_e32 v225, v225, v176
	v_cvt_i32_f32_e32 v225, v225
	v_mul_f32_e32 v226, v226, v176
	v_cvt_i32_f32_e32 v226, v226
	v_mul_f32_e32 v227, v227, v176
	v_cvt_i32_f32_e32 v227, v227
	v_mul_f32_e32 v228, v228, v176
	v_cvt_i32_f32_e32 v228, v228
	v_mul_f32_e32 v229, v229, v176
	v_cvt_i32_f32_e32 v229, v229
	v_mul_f32_e32 v230, v230, v176
	v_cvt_i32_f32_e32 v230, v230
	v_mul_f32_e32 v231, v231, v176
	v_cvt_i32_f32_e32 v231, v231
	v_mul_f32_e32 v232, v232, v176
	v_cvt_i32_f32_e32 v232, v232
	v_mul_f32_e32 v233, v233, v176
	v_cvt_i32_f32_e32 v233, v233
	v_mul_f32_e32 v234, v234, v176
	v_cvt_i32_f32_e32 v234, v234
	v_mul_f32_e32 v235, v235, v176
	v_cvt_i32_f32_e32 v235, v235
	v_mul_f32_e32 v236, v236, v177
	v_cvt_i32_f32_e32 v236, v236
	v_mul_f32_e32 v237, v237, v177
	v_cvt_i32_f32_e32 v237, v237
	v_mul_f32_e32 v238, v238, v177
	v_cvt_i32_f32_e32 v238, v238
	v_mul_f32_e32 v239, v239, v177
	v_cvt_i32_f32_e32 v239, v239
	ds_add_u32 v167, v224 offset:3072
	ds_add_u32 v167, v225 offset:3264
	ds_add_u32 v167, v226 offset:3456
	ds_add_u32 v167, v227 offset:3648
	ds_add_u32 v167, v228 offset:3136
	ds_add_u32 v167, v229 offset:3328
	ds_add_u32 v167, v230 offset:3520
	ds_add_u32 v167, v231 offset:3712
; __global__ void __launch_bounds__(512, 2) hymba_fwd(Args args) {
;     ...
;                     for (int s4 = 0; s4 < 4; ++s4)
; #pragma unroll
;                         for (int x = 0; x < 2; ++x) { const bf16x8 xh = __builtin_bit_cast(bf16x8, xa[x][s4]);
; #pragma unroll
;                             for (int nt = 0; nt < 3; ++nt) {
;                                 acc[x][nt] = __builtin_amdgcn_mfma_f32_16x16x32_bf16(xh, bl[s4][nt], acc[x][nt], 0, 0, 0);
;                                 acc[x][nt] = __builtin_amdgcn_mfma_f32_16x16x32_bf16(xh, bh[s4][nt], acc[x][nt], 0, 0, 0); } }
;                 }
; #pragma unroll
;                 for (int x = 0; x < 2; ++x) {
; #pragma unroll
;                     for (int nt = 0; nt < 3; ++nt)
; #pragma unroll
;                         for (int e = 0; e < 4; ++e) part[(wave * 32 + 16 * x + 4 * kg + e) * 48 + 16 * nt + li] = acc[x][nt][e];
;                     float s1 = ss[x]; s1 += __shfl_xor(s1, 16); s1 += __shfl_xor(s1, 32);
;                     if (kg == 0) ssp[wave * 32 + 16 * x + li] = s1; }
	ds_add_u32 v167, v232 offset:3200
	ds_add_u32 v167, v233 offset:3392
	ds_add_u32 v167, v234 offset:3584
	ds_add_u32 v167, v235 offset:3776
	s_mov_b64 exec, s[12:13]
	ds_add_u32 v168, v236 offset:49216
	s_mov_b64 exec, s[16:17]
	ds_add_u32 v168, v237 offset:49216
	s_mov_b64 exec, s[20:21]
	ds_add_u32 v168, v238 offset:49216
	s_mov_b64 exec, s[22:23]
	ds_add_u32 v168, v239 offset:49216
	s_mov_b64 exec, -1
	v_mfma_f32_16x16x32_bf16 v[224:227], v[92:95], v[180:183], 0
	v_mfma_f32_16x16x32_bf16 v[224:227], v[92:95], v[184:187], v[224:227]
	v_mfma_f32_16x16x32_bf16 v[224:227], v[84:87], v[204:207], v[224:227]
	v_mfma_f32_16x16x32_bf16 v[224:227], v[84:87], v[148:151], v[224:227]
	v_mfma_f32_16x16x32_bf16 v[228:231], v[92:95], v[188:191], 0
	v_mfma_f32_16x16x32_bf16 v[228:231], v[92:95], v[192:195], v[228:231]
	v_mfma_f32_16x16x32_bf16 v[228:231], v[84:87], v[208:211], v[228:231]
	v_mfma_f32_16x16x32_bf16 v[228:231], v[84:87], v[212:215], v[228:231]
	v_mfma_f32_16x16x32_bf16 v[232:235], v[92:95], v[196:199], 0
	v_mfma_f32_16x16x32_bf16 v[232:235], v[92:95], v[200:203], v[232:235]
	v_mfma_f32_16x16x32_bf16 v[232:235], v[84:87], v[216:219], v[232:235]
	v_mfma_f32_16x16x32_bf16 v[232:235], v[84:87], v[220:223], v[232:235]
	v_mfma_f32_16x16x32_bf16 v[236:239], v[92:95], v[92:95], 0
	v_mfma_f32_16x16x32_bf16 v[236:239], v[84:87], v[84:87], v[236:239]
	s_nop 7
	s_nop 3
	v_mul_f32_e32 v224, v224, v176
	v_cvt_i32_f32_e32 v224, v224
	v_mul_f32_e32 v225, v225, v176
	v_cvt_i32_f32_e32 v225, v225
	v_mul_f32_e32 v226, v226, v176
	v_cvt_i32_f32_e32 v226, v226
	v_mul_f32_e32 v227, v227, v176
	v_cvt_i32_f32_e32 v227, v227
	v_mul_f32_e32 v228, v228, v176
	v_cvt_i32_f32_e32 v228, v228
	v_mul_f32_e32 v229, v229, v176
	v_cvt_i32_f32_e32 v229, v229
	v_mul_f32_e32 v230, v230, v176
	v_cvt_i32_f32_e32 v230, v230
	v_mul_f32_e32 v231, v231, v176
	v_cvt_i32_f32_e32 v231, v231
	v_mul_f32_e32 v232, v232, v176
	v_cvt_i32_f32_e32 v232, v232
	v_mul_f32_e32 v233, v233, v176
	v_cvt_i32_f32_e32 v233, v233
	v_mul_f32_e32 v234, v234, v176
	v_cvt_i32_f32_e32 v234, v234
	v_mul_f32_e32 v235, v235, v176
	v_cvt_i32_f32_e32 v235, v235
	v_mul_f32_e32 v236, v236, v177
	v_cvt_i32_f32_e32 v236, v236
	v_mul_f32_e32 v237, v237, v177
	v_cvt_i32_f32_e32 v237, v237
	v_mul_f32_e32 v238, v238, v177
	v_cvt_i32_f32_e32 v238, v238
	v_mul_f32_e32 v239, v239, v177
	v_cvt_i32_f32_e32 v239, v239
	ds_add_u32 v167, v224 offset:6144
	ds_add_u32 v167, v225 offset:6336
	ds_add_u32 v167, v226 offset:6528
	ds_add_u32 v167, v227 offset:6720
	ds_add_u32 v167, v228 offset:6208
	ds_add_u32 v167, v229 offset:6400
	ds_add_u32 v167, v230 offset:6592
	ds_add_u32 v167, v231 offset:6784
	ds_add_u32 v167, v232 offset:6272
	ds_add_u32 v167, v233 offset:6464
	ds_add_u32 v167, v234 offset:6656
	ds_add_u32 v167, v235 offset:6848
	s_mov_b64 exec, s[12:13]
	ds_add_u32 v168, v236 offset:49280
	s_mov_b64 exec, s[16:17]
	ds_add_u32 v168, v237 offset:49280
	s_mov_b64 exec, s[20:21]
	ds_add_u32 v168, v238 offset:49280
	s_mov_b64 exec, s[22:23]
	ds_add_u32 v168, v239 offset:49280
	s_mov_b64 exec, -1
	v_mfma_f32_16x16x32_bf16 v[224:227], v[76:79], v[180:183], 0
	v_mfma_f32_16x16x32_bf16 v[224:227], v[76:79], v[184:187], v[224:227]
	v_mfma_f32_16x16x32_bf16 v[224:227], v[68:71], v[204:207], v[224:227]
	v_mfma_f32_16x16x32_bf16 v[224:227], v[68:71], v[148:151], v[224:227]
	v_mfma_f32_16x16x32_bf16 v[228:231], v[76:79], v[188:191], 0
	v_mfma_f32_16x16x32_bf16 v[228:231], v[76:79], v[192:195], v[228:231]
	v_mfma_f32_16x16x32_bf16 v[228:231], v[68:71], v[208:211], v[228:231]
	v_mfma_f32_16x16x32_bf16 v[228:231], v[68:71], v[212:215], v[228:231]
	v_mfma_f32_16x16x32_bf16 v[232:235], v[76:79], v[196:199], 0
	v_mfma_f32_16x16x32_bf16 v[232:235], v[76:79], v[200:203], v[232:235]
	v_mfma_f32_16x16x32_bf16 v[232:235], v[68:71], v[216:219], v[232:235]
	v_mfma_f32_16x16x32_bf16 v[232:235], v[68:71], v[220:223], v[232:235]
	v_mfma_f32_16x16x32_bf16 v[236:239], v[76:79], v[76:79], 0
	v_mfma_f32_16x16x32_bf16 v[236:239], v[68:71], v[68:71], v[236:239]
	s_nop 7
	s_nop 3
	v_mul_f32_e32 v224, v224, v176
	v_cvt_i32_f32_e32 v224, v224
	v_mul_f32_e32 v225, v225, v176
	v_cvt_i32_f32_e32 v225, v225
	v_mul_f32_e32 v226, v226, v176
	v_cvt_i32_f32_e32 v226, v226
	v_mul_f32_e32 v227, v227, v176
	v_cvt_i32_f32_e32 v227, v227
	v_mul_f32_e32 v228, v228, v176
	v_cvt_i32_f32_e32 v228, v228
	v_mul_f32_e32 v229, v229, v176
	v_cvt_i32_f32_e32 v229, v229
	v_mul_f32_e32 v230, v230, v176
	v_cvt_i32_f32_e32 v230, v230
	v_mul_f32_e32 v231, v231, v176
	v_cvt_i32_f32_e32 v231, v231
	v_mul_f32_e32 v232, v232, v176
	v_cvt_i32_f32_e32 v232, v232
	v_mul_f32_e32 v233, v233, v176
	v_cvt_i32_f32_e32 v233, v233
	v_mul_f32_e32 v234, v234, v176
	v_cvt_i32_f32_e32 v234, v234
	v_mul_f32_e32 v235, v235, v176
	v_cvt_i32_f32_e32 v235, v235
	v_mul_f32_e32 v236, v236, v177
	v_cvt_i32_f32_e32 v236, v236
	v_mul_f32_e32 v237, v237, v177
	v_cvt_i32_f32_e32 v237, v237
	v_mul_f32_e32 v238, v238, v177
	v_cvt_i32_f32_e32 v238, v238
	v_mul_f32_e32 v239, v239, v177
	v_cvt_i32_f32_e32 v239, v239
	ds_add_u32 v167, v224 offset:9216
	ds_add_u32 v167, v225 offset:9408
	ds_add_u32 v167, v226 offset:9600
	ds_add_u32 v167, v227 offset:9792
	ds_add_u32 v167, v228 offset:9280
	ds_add_u32 v167, v229 offset:9472
	ds_add_u32 v167, v230 offset:9664
	ds_add_u32 v167, v231 offset:9856
	ds_add_u32 v167, v232 offset:9344
	ds_add_u32 v167, v233 offset:9536
	ds_add_u32 v167, v234 offset:9728
	ds_add_u32 v167, v235 offset:9920
	s_mov_b64 exec, s[12:13]
	ds_add_u32 v168, v236 offset:49344
	s_mov_b64 exec, s[16:17]
	ds_add_u32 v168, v237 offset:49344
	s_mov_b64 exec, s[20:21]
	ds_add_u32 v168, v238 offset:49344
; __global__ void __launch_bounds__(512, 2) hymba_fwd(Args args) {
;     ...
;                     for (int s4 = 0; s4 < 4; ++s4)
; #pragma unroll
;                         for (int x = 0; x < 2; ++x) { const bf16x8 xh = __builtin_bit_cast(bf16x8, xa[x][s4]);
; #pragma unroll
;                             for (int nt = 0; nt < 3; ++nt) {
;                                 acc[x][nt] = __builtin_amdgcn_mfma_f32_16x16x32_bf16(xh, bl[s4][nt], acc[x][nt], 0, 0, 0);
;                                 acc[x][nt] = __builtin_amdgcn_mfma_f32_16x16x32_bf16(xh, bh[s4][nt], acc[x][nt], 0, 0, 0); } }
;                 }
; #pragma unroll
;                 for (int x = 0; x < 2; ++x) {
; #pragma unroll
;                     for (int nt = 0; nt < 3; ++nt)
; #pragma unroll
;                         for (int e = 0; e < 4; ++e) part[(wave * 32 + 16 * x + 4 * kg + e) * 48 + 16 * nt + li] = acc[x][nt][e];
;                     float s1 = ss[x]; s1 += __shfl_xor(s1, 16); s1 += __shfl_xor(s1, 32);
;                     if (kg == 0) ssp[wave * 32 + 16 * x + li] = s1; }
	s_mov_b64 exec, s[22:23]
	ds_add_u32 v168, v239 offset:49344
	s_mov_b64 exec, -1
	v_mfma_f32_16x16x32_bf16 v[224:227], v[60:63], v[180:183], 0
	v_mfma_f32_16x16x32_bf16 v[224:227], v[60:63], v[184:187], v[224:227]
	v_mfma_f32_16x16x32_bf16 v[224:227], v[52:55], v[204:207], v[224:227]
	v_mfma_f32_16x16x32_bf16 v[224:227], v[52:55], v[148:151], v[224:227]
	v_mfma_f32_16x16x32_bf16 v[228:231], v[60:63], v[188:191], 0
	v_mfma_f32_16x16x32_bf16 v[228:231], v[60:63], v[192:195], v[228:231]
	v_mfma_f32_16x16x32_bf16 v[228:231], v[52:55], v[208:211], v[228:231]
	v_mfma_f32_16x16x32_bf16 v[228:231], v[52:55], v[212:215], v[228:231]
	v_mfma_f32_16x16x32_bf16 v[232:235], v[60:63], v[196:199], 0
	v_mfma_f32_16x16x32_bf16 v[232:235], v[60:63], v[200:203], v[232:235]
	v_mfma_f32_16x16x32_bf16 v[232:235], v[52:55], v[216:219], v[232:235]
	v_mfma_f32_16x16x32_bf16 v[232:235], v[52:55], v[220:223], v[232:235]
	v_mfma_f32_16x16x32_bf16 v[236:239], v[60:63], v[60:63], 0
	v_mfma_f32_16x16x32_bf16 v[236:239], v[52:55], v[52:55], v[236:239]
	s_nop 7
	s_nop 3
	v_mul_f32_e32 v224, v224, v176
	v_cvt_i32_f32_e32 v224, v224
	v_mul_f32_e32 v225, v225, v176
	v_cvt_i32_f32_e32 v225, v225
	v_mul_f32_e32 v226, v226, v176
	v_cvt_i32_f32_e32 v226, v226
	v_mul_f32_e32 v227, v227, v176
	v_cvt_i32_f32_e32 v227, v227
	v_mul_f32_e32 v228, v228, v176
	v_cvt_i32_f32_e32 v228, v228
	v_mul_f32_e32 v229, v229, v176
	v_cvt_i32_f32_e32 v229, v229
	v_mul_f32_e32 v230, v230, v176
	v_cvt_i32_f32_e32 v230, v230
	v_mul_f32_e32 v231, v231, v176
	v_cvt_i32_f32_e32 v231, v231
	v_mul_f32_e32 v232, v232, v176
	v_cvt_i32_f32_e32 v232, v232
	v_mul_f32_e32 v233, v233, v176
	v_cvt_i32_f32_e32 v233, v233
	v_mul_f32_e32 v234, v234, v176
	v_cvt_i32_f32_e32 v234, v234
	v_mul_f32_e32 v235, v235, v176
	v_cvt_i32_f32_e32 v235, v235
	v_mul_f32_e32 v236, v236, v177
	v_cvt_i32_f32_e32 v236, v236
	v_mul_f32_e32 v237, v237, v177
	v_cvt_i32_f32_e32 v237, v237
	v_mul_f32_e32 v238, v238, v177
	v_cvt_i32_f32_e32 v238, v238
	v_mul_f32_e32 v239, v239, v177
	v_cvt_i32_f32_e32 v239, v239
	ds_add_u32 v167, v224 offset:24576
	ds_add_u32 v167, v225 offset:24768
	ds_add_u32 v167, v226 offset:24960
	ds_add_u32 v167, v227 offset:25152
	ds_add_u32 v167, v228 offset:24640
	ds_add_u32 v167, v229 offset:24832
	ds_add_u32 v167, v230 offset:25024
	ds_add_u32 v167, v231 offset:25216
	ds_add_u32 v167, v232 offset:24704
	ds_add_u32 v167, v233 offset:24896
	ds_add_u32 v167, v234 offset:25088
	ds_add_u32 v167, v235 offset:25280
	s_mov_b64 exec, s[12:13]
	ds_add_u32 v168, v236 offset:49664
	s_mov_b64 exec, s[16:17]
	ds_add_u32 v168, v237 offset:49664
	s_mov_b64 exec, s[20:21]
	ds_add_u32 v168, v238 offset:49664
	s_mov_b64 exec, s[22:23]
	ds_add_u32 v168, v239 offset:49664
	s_mov_b64 exec, -1
	v_mfma_f32_16x16x32_bf16 v[224:227], v[44:47], v[180:183], 0
	v_mfma_f32_16x16x32_bf16 v[224:227], v[44:47], v[184:187], v[224:227]
	v_mfma_f32_16x16x32_bf16 v[224:227], v[36:39], v[204:207], v[224:227]
	v_mfma_f32_16x16x32_bf16 v[224:227], v[36:39], v[148:151], v[224:227]
	v_mfma_f32_16x16x32_bf16 v[228:231], v[44:47], v[188:191], 0
	v_mfma_f32_16x16x32_bf16 v[228:231], v[44:47], v[192:195], v[228:231]
	v_mfma_f32_16x16x32_bf16 v[228:231], v[36:39], v[208:211], v[228:231]
	v_mfma_f32_16x16x32_bf16 v[228:231], v[36:39], v[212:215], v[228:231]
	v_mfma_f32_16x16x32_bf16 v[232:235], v[44:47], v[196:199], 0
	v_mfma_f32_16x16x32_bf16 v[232:235], v[44:47], v[200:203], v[232:235]
	v_mfma_f32_16x16x32_bf16 v[232:235], v[36:39], v[216:219], v[232:235]
	v_mfma_f32_16x16x32_bf16 v[232:235], v[36:39], v[220:223], v[232:235]
	v_mfma_f32_16x16x32_bf16 v[236:239], v[44:47], v[44:47], 0
	v_mfma_f32_16x16x32_bf16 v[236:239], v[36:39], v[36:39], v[236:239]
	s_nop 7
	s_nop 3
	v_mul_f32_e32 v224, v224, v176
	v_cvt_i32_f32_e32 v224, v224
	v_mul_f32_e32 v225, v225, v176
	v_cvt_i32_f32_e32 v225, v225
	v_mul_f32_e32 v226, v226, v176
	v_cvt_i32_f32_e32 v226, v226
	v_mul_f32_e32 v227, v227, v176
	v_cvt_i32_f32_e32 v227, v227
	v_mul_f32_e32 v228, v228, v176
	v_cvt_i32_f32_e32 v228, v228
	v_mul_f32_e32 v229, v229, v176
	v_cvt_i32_f32_e32 v229, v229
	v_mul_f32_e32 v230, v230, v176
	v_cvt_i32_f32_e32 v230, v230
	v_mul_f32_e32 v231, v231, v176
	v_cvt_i32_f32_e32 v231, v231
	v_mul_f32_e32 v232, v232, v176
	v_cvt_i32_f32_e32 v232, v232
	v_mul_f32_e32 v233, v233, v176
	v_cvt_i32_f32_e32 v233, v233
	v_mul_f32_e32 v234, v234, v176
	v_cvt_i32_f32_e32 v234, v234
	v_mul_f32_e32 v235, v235, v176
	v_cvt_i32_f32_e32 v235, v235
	v_mul_f32_e32 v236, v236, v177
	v_cvt_i32_f32_e32 v236, v236
	v_mul_f32_e32 v237, v237, v177
	v_cvt_i32_f32_e32 v237, v237
	v_mul_f32_e32 v238, v238, v177
	v_cvt_i32_f32_e32 v238, v238
	v_mul_f32_e32 v239, v239, v177
	v_cvt_i32_f32_e32 v239, v239
	ds_add_u32 v167, v224 offset:27648
	ds_add_u32 v167, v225 offset:27840
	ds_add_u32 v167, v226 offset:28032
	ds_add_u32 v167, v227 offset:28224
	ds_add_u32 v167, v228 offset:27712
	ds_add_u32 v167, v229 offset:27904
	ds_add_u32 v167, v230 offset:28096
	ds_add_u32 v167, v231 offset:28288
	ds_add_u32 v167, v232 offset:27776
	ds_add_u32 v167, v233 offset:27968
	ds_add_u32 v167, v234 offset:28160
	ds_add_u32 v167, v235 offset:28352
	s_mov_b64 exec, s[12:13]
	ds_add_u32 v168, v236 offset:49728
	s_mov_b64 exec, s[16:17]
	ds_add_u32 v168, v237 offset:49728
	s_mov_b64 exec, s[20:21]
	ds_add_u32 v168, v238 offset:49728
	s_mov_b64 exec, s[22:23]
	ds_add_u32 v168, v239 offset:49728
	s_mov_b64 exec, -1
	v_mfma_f32_16x16x32_bf16 v[224:227], v[20:23], v[180:183], 0
	v_mfma_f32_16x16x32_bf16 v[224:227], v[20:23], v[184:187], v[224:227]
	v_mfma_f32_16x16x32_bf16 v[224:227], v[24:27], v[204:207], v[224:227]
; __global__ void __launch_bounds__(512, 2) hymba_fwd(Args args) {
;     ...
;                     for (int s4 = 0; s4 < 4; ++s4)
; #pragma unroll
;                         for (int x = 0; x < 2; ++x) { const bf16x8 xh = __builtin_bit_cast(bf16x8, xa[x][s4]);
; #pragma unroll
;                             for (int nt = 0; nt < 3; ++nt) {
;                                 acc[x][nt] = __builtin_amdgcn_mfma_f32_16x16x32_bf16(xh, bl[s4][nt], acc[x][nt], 0, 0, 0);
;                                 acc[x][nt] = __builtin_amdgcn_mfma_f32_16x16x32_bf16(xh, bh[s4][nt], acc[x][nt], 0, 0, 0); } }
;                 }
; #pragma unroll
;                 for (int x = 0; x < 2; ++x) {
; #pragma unroll
;                     for (int nt = 0; nt < 3; ++nt)
; #pragma unroll
;                         for (int e = 0; e < 4; ++e) part[(wave * 32 + 16 * x + 4 * kg + e) * 48 + 16 * nt + li] = acc[x][nt][e];
;                     float s1 = ss[x]; s1 += __shfl_xor(s1, 16); s1 += __shfl_xor(s1, 32);
;                     if (kg == 0) ssp[wave * 32 + 16 * x + li] = s1; }
	v_mfma_f32_16x16x32_bf16 v[224:227], v[24:27], v[148:151], v[224:227]
	v_mfma_f32_16x16x32_bf16 v[228:231], v[20:23], v[188:191], 0
	v_mfma_f32_16x16x32_bf16 v[228:231], v[20:23], v[192:195], v[228:231]
	v_mfma_f32_16x16x32_bf16 v[228:231], v[24:27], v[208:211], v[228:231]
	v_mfma_f32_16x16x32_bf16 v[228:231], v[24:27], v[212:215], v[228:231]
	v_mfma_f32_16x16x32_bf16 v[232:235], v[20:23], v[196:199], 0
	v_mfma_f32_16x16x32_bf16 v[232:235], v[20:23], v[200:203], v[232:235]
	v_mfma_f32_16x16x32_bf16 v[232:235], v[24:27], v[216:219], v[232:235]
	v_mfma_f32_16x16x32_bf16 v[232:235], v[24:27], v[220:223], v[232:235]
	v_mfma_f32_16x16x32_bf16 v[236:239], v[20:23], v[20:23], 0
	v_mfma_f32_16x16x32_bf16 v[236:239], v[24:27], v[24:27], v[236:239]
	s_nop 7
	s_nop 3
	v_mul_f32_e32 v224, v224, v176
	v_cvt_i32_f32_e32 v224, v224
	v_mul_f32_e32 v225, v225, v176
	v_cvt_i32_f32_e32 v225, v225
	v_mul_f32_e32 v226, v226, v176
	v_cvt_i32_f32_e32 v226, v226
	v_mul_f32_e32 v227, v227, v176
	v_cvt_i32_f32_e32 v227, v227
	v_mul_f32_e32 v228, v228, v176
	v_cvt_i32_f32_e32 v228, v228
	v_mul_f32_e32 v229, v229, v176
	v_cvt_i32_f32_e32 v229, v229
	v_mul_f32_e32 v230, v230, v176
	v_cvt_i32_f32_e32 v230, v230
	v_mul_f32_e32 v231, v231, v176
	v_cvt_i32_f32_e32 v231, v231
	v_mul_f32_e32 v232, v232, v176
	v_cvt_i32_f32_e32 v232, v232
	v_mul_f32_e32 v233, v233, v176
	v_cvt_i32_f32_e32 v233, v233
	v_mul_f32_e32 v234, v234, v176
	v_cvt_i32_f32_e32 v234, v234
	v_mul_f32_e32 v235, v235, v176
	v_cvt_i32_f32_e32 v235, v235
	v_mul_f32_e32 v236, v236, v177
	v_cvt_i32_f32_e32 v236, v236
	v_mul_f32_e32 v237, v237, v177
	v_cvt_i32_f32_e32 v237, v237
	v_mul_f32_e32 v238, v238, v177
	v_cvt_i32_f32_e32 v238, v238
	v_mul_f32_e32 v239, v239, v177
	v_cvt_i32_f32_e32 v239, v239
	ds_add_u32 v167, v224 offset:30720
	ds_add_u32 v167, v225 offset:30912
	ds_add_u32 v167, v226 offset:31104
	ds_add_u32 v167, v227 offset:31296
	ds_add_u32 v167, v228 offset:30784
	ds_add_u32 v167, v229 offset:30976
	ds_add_u32 v167, v230 offset:31168
	ds_add_u32 v167, v231 offset:31360
	ds_add_u32 v167, v232 offset:30848
	ds_add_u32 v167, v233 offset:31040
	ds_add_u32 v167, v234 offset:31232
	ds_add_u32 v167, v235 offset:31424
	s_mov_b64 exec, s[12:13]
	ds_add_u32 v168, v236 offset:49792
	s_mov_b64 exec, s[16:17]
	ds_add_u32 v168, v237 offset:49792
	s_mov_b64 exec, s[20:21]
	ds_add_u32 v168, v238 offset:49792
	s_mov_b64 exec, s[22:23]
	ds_add_u32 v168, v239 offset:49792
	s_mov_b64 exec, -1
	v_mfma_f32_16x16x32_bf16 v[224:227], v[4:7], v[180:183], 0
	v_mfma_f32_16x16x32_bf16 v[224:227], v[4:7], v[184:187], v[224:227]
	v_mfma_f32_16x16x32_bf16 v[224:227], v[8:11], v[204:207], v[224:227]
	v_mfma_f32_16x16x32_bf16 v[224:227], v[8:11], v[148:151], v[224:227]
	v_mfma_f32_16x16x32_bf16 v[228:231], v[4:7], v[188:191], 0
	v_mfma_f32_16x16x32_bf16 v[228:231], v[4:7], v[192:195], v[228:231]
	v_mfma_f32_16x16x32_bf16 v[228:231], v[8:11], v[208:211], v[228:231]
	v_mfma_f32_16x16x32_bf16 v[228:231], v[8:11], v[212:215], v[228:231]
	v_mfma_f32_16x16x32_bf16 v[232:235], v[4:7], v[196:199], 0
	v_mfma_f32_16x16x32_bf16 v[232:235], v[4:7], v[200:203], v[232:235]
	v_mfma_f32_16x16x32_bf16 v[232:235], v[8:11], v[216:219], v[232:235]
	v_mfma_f32_16x16x32_bf16 v[232:235], v[8:11], v[220:223], v[232:235]
	v_mfma_f32_16x16x32_bf16 v[236:239], v[4:7], v[4:7], 0
	v_mfma_f32_16x16x32_bf16 v[236:239], v[8:11], v[8:11], v[236:239]
	s_nop 7
	s_nop 3
	v_mul_f32_e32 v224, v224, v176
	v_cvt_i32_f32_e32 v224, v224
	v_mul_f32_e32 v225, v225, v176
	v_cvt_i32_f32_e32 v225, v225
	v_mul_f32_e32 v226, v226, v176
	v_cvt_i32_f32_e32 v226, v226
	v_mul_f32_e32 v227, v227, v176
	v_cvt_i32_f32_e32 v227, v227
	v_mul_f32_e32 v228, v228, v176
	v_cvt_i32_f32_e32 v228, v228
	v_mul_f32_e32 v229, v229, v176
	v_cvt_i32_f32_e32 v229, v229
	v_mul_f32_e32 v230, v230, v176
	v_cvt_i32_f32_e32 v230, v230
	v_mul_f32_e32 v231, v231, v176
	v_cvt_i32_f32_e32 v231, v231
	v_mul_f32_e32 v232, v232, v176
	v_cvt_i32_f32_e32 v232, v232
	v_mul_f32_e32 v233, v233, v176
	v_cvt_i32_f32_e32 v233, v233
	v_mul_f32_e32 v234, v234, v176
	v_cvt_i32_f32_e32 v234, v234
	v_mul_f32_e32 v235, v235, v176
	v_cvt_i32_f32_e32 v235, v235
	v_mul_f32_e32 v236, v236, v177
	v_cvt_i32_f32_e32 v236, v236
	v_mul_f32_e32 v237, v237, v177
	v_cvt_i32_f32_e32 v237, v237
	v_mul_f32_e32 v238, v238, v177
	v_cvt_i32_f32_e32 v238, v238
	v_mul_f32_e32 v239, v239, v177
	v_cvt_i32_f32_e32 v239, v239
	ds_add_u32 v167, v224 offset:33792
	ds_add_u32 v167, v225 offset:33984
	ds_add_u32 v167, v226 offset:34176
	ds_add_u32 v167, v227 offset:34368
	ds_add_u32 v167, v228 offset:33856
	ds_add_u32 v167, v229 offset:34048
	ds_add_u32 v167, v230 offset:34240
	ds_add_u32 v167, v231 offset:34432
	ds_add_u32 v167, v232 offset:33920
	ds_add_u32 v167, v233 offset:34112
	ds_add_u32 v167, v234 offset:34304
	ds_add_u32 v167, v235 offset:34496
	s_mov_b64 exec, s[12:13]
	ds_add_u32 v168, v236 offset:49856
	s_mov_b64 exec, s[16:17]
	ds_add_u32 v168, v237 offset:49856
	s_mov_b64 exec, s[20:21]
	ds_add_u32 v168, v238 offset:49856
	s_mov_b64 exec, s[22:23]
	ds_add_u32 v168, v239 offset:49856
	s_mov_b64 exec, -1
	s_waitcnt lgkmcnt(0)
	s_barrier
	ds_read_b128 v[180:183], v170 offset:0
	ds_read_b128 v[184:187], v170 offset:1024
	ds_read_b128 v[188:191], v170 offset:2048
	ds_read_b128 v[192:195], v170 offset:3072
	ds_read_b128 v[196:199], v170 offset:4096
	ds_read_b128 v[200:203], v170 offset:5120
	ds_read_b32 v204, v171 offset:49152
	s_lshl_b32 s33, s84, 13
	s_lshl_b32 s41, s48, 8
	s_add_i32 s33, s33, s41
	s_lshl_b32 s41, s100, 5
	s_add_i32 s33, s33, s41
	s_mul_i32 s41, s33, 0xc0
	s_add_u32 s12, s26, 0x15000000
	s_addc_u32 s13, s27, 0
	s_add_u32 s12, s12, s41
	s_addc_u32 s13, s13, 0
	v_lshlrev_b32_e32 v205, 4, v164
	s_waitcnt lgkmcnt(0)
	global_store_dwordx4 v205, v[180:183], s[12:13] sc0 sc1
	global_store_dwordx4 v205, v[184:187], s[12:13] offset:1024 sc0 sc1
	global_store_dwordx4 v205, v[188:191], s[12:13] offset:2048 sc0 sc1
	global_store_dwordx4 v205, v[192:195], s[12:13] offset:3072 sc0 sc1
	s_add_u32 s12, s12, 0x1000
	s_addc_u32 s13, s13, 0
	global_store_dwordx4 v205, v[196:199], s[12:13] sc0 sc1
	global_store_dwordx4 v205, v[200:203], s[12:13] offset:1024 sc0 sc1
	s_lshl_b32 s41, s33, 2
	s_add_u32 s12, s26, 0x16000000
	s_addc_u32 s13, s27, 0
	s_add_u32 s12, s12, s41
	s_addc_u32 s13, s13, 0
	v_lshlrev_b32_e32 v205, 2, v164
	s_mov_b32 exec_lo, -1
	s_mov_b32 exec_hi, 0
	global_store_dword v205, v204, s[12:13] sc0 sc1
	s_mov_b64 exec, -1
	v_mov_b64_e32 v[144:145], 0x100
	v_mov_b64_e32 v[146:147], 0xff
	s_andn2_b64 vcc, exec, s[0:1]
	s_mov_b64 s[0:1], -1
	s_cbranch_vccnz .LBB0_478
	s_andn2_b64 vcc, exec, s[4:5]
	s_cbranch_vccnz .LBB0_477
	s_barrier
	s_branch .LBB0_477

; __device__ __forceinline__ unsigned xb_add(unsigned* p, unsigned v) { return __hip_atomic_fetch_add(p, v, __ATOMIC_RELAXED, __HIP_MEMORY_SCOPE_AGENT); }
; __device__ __forceinline__ void xcd_barrier(const XcdBarrier& b, const int tid) {
;     ...
;         if (old + 1u == (gen + 1u) * nloc) {
;             __builtin_amdgcn_fence(__ATOMIC_RELEASE, "agent");
;             asm volatile("s_waitcnt vmcnt(0)" ::: "memory");
;             const unsigned og = xb_add(&bar[XB_TOP], 1u);
;             const unsigned tg = og / nx;
;             if (og + 1u == (tg + 1u) * nx) xb_add(&bar[XB_TOPGEN], 1u);
.LBB0_526:
	s_andn2_saveexec_b64 s[6:7], s[6:7]
	s_cbranch_execz .LBB0_546
	s_mov_b64 s[6:7], exec
	s_waitcnt lgkmcnt(0)
	s_waitcnt vmcnt(0)
	v_mbcnt_lo_u32_b32 v1, s6, 0
	v_mbcnt_hi_u32_b32 v1, s7, v1
	v_cmp_eq_u32_e32 vcc, 0, v1
	s_and_saveexec_b64 s[8:9], vcc
	s_cbranch_execz .LBB0_529
	s_bcnt1_i32_b64 s6, s[6:7]
	v_mov_b32_e32 v2, 0x3000
	v_mov_b32_e32 v3, s6
	global_atomic_add v2, v2, v3, s[26:27] offset:1024 sc0

; __global__ void __launch_bounds__(512, 2) hymba_fwd(Args args) {
;     ...
;             {
;                 const bf16* xp = X1B + (size_t)(t0 + li) * DM + 256 * wave + 8 * kg;
;                 const bf16* hp = WRH + (size_t)li * DM + 256 * wave + 8 * kg; const bf16* lp = WRL + (size_t)li * DM + 256 * wave + 8 * kg;
;                 f32x4 acc[2][3]; float ss[2] = {0.f, 0.f};
; #pragma unroll
;                 for (int x = 0; x < 2; ++x)
; #pragma unroll
;                     for (int nt = 0; nt < 3; ++nt) acc[x][nt] = (f32x4){0.f, 0.f, 0.f, 0.f};
; #pragma unroll 1
;                 for (int hf = 0; hf < 2; ++hf) {
;                     v4u xa[2][4]; bf16x8 bh[4][3], bl[4][3];
; #pragma unroll
;                     for (int s4 = 0; s4 < 4; ++s4) { const int ko = 32 * (4 * hf + s4);
; #pragma unroll
;                         for (int x = 0; x < 2; ++x) xa[x][s4] = *(const v4u*)(xp + (size_t)(16 * x) * DM + ko);
; #pragma unroll
;                         for (int nt = 0; nt < 3; ++nt) { bh[s4][nt] = *(const bf16x8*)(hp + (size_t)(16 * nt) * DM + ko); bl[s4][nt] = *(const bf16x8*)(lp + (size_t)(16 * nt) * DM + ko); } }
;                     asm volatile("s_waitcnt vmcnt(0)" ::: "memory"); __builtin_amdgcn_sched_barrier(0);
; #pragma unroll
;                     for (int s4 = 0; s4 < 4; ++s4)
; #pragma unroll
;                         for (int x = 0; x < 2; ++x) { const v4u q = xa[x][s4];
;                             ss[x] += (bf_lo(q.x) * bf_lo(q.x) + bf_hi(q.x) * bf_hi(q.x)) + (bf_lo(q.y) * bf_lo(q.y) + bf_hi(q.y) * bf_hi(q.y)) + (bf_lo(q.z) * bf_lo(q.z) + bf_hi(q.z) * bf_hi(q.z)) + (bf_lo(q.w) * bf_lo(q.w) + bf_hi(q.w) * bf_hi(q.w)); }
;                     __builtin_amdgcn_sched_barrier(0);
; #pragma unroll
;                     for (int s4 = 0; s4 < 4; ++s4)
; #pragma unroll
;                         for (int x = 0; x < 2; ++x) { const bf16x8 xh = __builtin_bit_cast(bf16x8, xa[x][s4]);
; #pragma unroll
;                             for (int nt = 0; nt < 3; ++nt) {
;                                 acc[x][nt] = __builtin_amdgcn_mfma_f32_16x16x32_bf16(xh, bl[s4][nt], acc[x][nt], 0, 0, 0);
;                                 acc[x][nt] = __builtin_amdgcn_mfma_f32_16x16x32_bf16(xh, bh[s4][nt], acc[x][nt], 0, 0, 0); } }
;                 }
; #pragma unroll
;                 for (int x = 0; x < 2; ++x) {
; #pragma unroll
.LBB0_553:
	s_lshl_b32 s33, s66, 5
	s_lshl_b32 s16, s92, 13
	s_add_i32 s16, s16, s33
	s_mul_i32 s17, s16, 0xc0
	s_add_u32 s20, s26, 0x15000000
	s_addc_u32 s21, s27, 0
	s_add_u32 s20, s20, s17
	s_addc_u32 s21, s21, 0
	v_mbcnt_lo_u32_b32 v0, -1, 0
	v_mbcnt_hi_u32_b32 v0, -1, v0
	v_lshlrev_b32_e32 v1, 4, v0
	global_load_dwordx4 v[8:11], v1, s[20:21] sc0 sc1
	global_load_dwordx4 v[12:15], v1, s[20:21] offset:1024 sc0 sc1
	global_load_dwordx4 v[16:19], v1, s[20:21] offset:2048 sc0 sc1
	global_load_dwordx4 v[20:23], v1, s[20:21] offset:3072 sc0 sc1
	s_add_u32 s20, s20, 0x1000
	s_addc_u32 s21, s21, 0
	global_load_dwordx4 v[24:27], v1, s[20:21] sc0 sc1
	global_load_dwordx4 v[28:31], v1, s[20:21] offset:1024 sc0 sc1
	s_lshl_b32 s17, s16, 2
	s_add_u32 s20, s26, 0x16000000
	s_addc_u32 s21, s27, 0
	s_add_u32 s20, s20, s17
	s_addc_u32 s21, s21, 0
	v_lshlrev_b32_e32 v2, 2, v0
	global_load_dword v3, v2, s[20:21] sc0 sc1
	s_mul_i32 s17, s92, 0x1800
	v_add_u32_e32 v4, s17, v1
	s_lshl_b32 s17, s92, 7
	v_add_u32_e32 v5, s17, v2
	v_mov_b32_e32 v6, 0x33800000
	v_mov_b32_e32 v7, 0x37800000
	s_waitcnt vmcnt(0)
	v_cvt_f32_i32_e32 v8, v8
	v_cvt_f32_i32_e32 v9, v9
	v_cvt_f32_i32_e32 v10, v10
	v_cvt_f32_i32_e32 v11, v11
	v_cvt_f32_i32_e32 v12, v12
	v_cvt_f32_i32_e32 v13, v13
	v_cvt_f32_i32_e32 v14, v14
	v_cvt_f32_i32_e32 v15, v15
	v_cvt_f32_i32_e32 v16, v16
	v_cvt_f32_i32_e32 v17, v17
	v_cvt_f32_i32_e32 v18, v18
	v_cvt_f32_i32_e32 v19, v19
	v_cvt_f32_i32_e32 v20, v20
	v_cvt_f32_i32_e32 v21, v21
	v_cvt_f32_i32_e32 v22, v22
	v_cvt_f32_i32_e32 v23, v23
	v_cvt_f32_i32_e32 v24, v24
	v_cvt_f32_i32_e32 v25, v25
	v_cvt_f32_i32_e32 v26, v26
	v_cvt_f32_i32_e32 v27, v27
	v_cvt_f32_i32_e32 v28, v28
	v_cvt_f32_i32_e32 v29, v29
	v_cvt_f32_i32_e32 v30, v30
	v_cvt_f32_i32_e32 v31, v31
	v_mul_f32_e32 v8, v8, v6
	v_mul_f32_e32 v9, v9, v6
	v_mul_f32_e32 v10, v10, v6
	v_mul_f32_e32 v11, v11, v6
	v_mul_f32_e32 v12, v12, v6
	v_mul_f32_e32 v13, v13, v6
	v_mul_f32_e32 v14, v14, v6
	v_mul_f32_e32 v15, v15, v6
	v_mul_f32_e32 v16, v16, v6
	v_mul_f32_e32 v17, v17, v6
	v_mul_f32_e32 v18, v18, v6
	v_mul_f32_e32 v19, v19, v6
	v_mul_f32_e32 v20, v20, v6
	v_mul_f32_e32 v21, v21, v6
	v_mul_f32_e32 v22, v22, v6
	v_mul_f32_e32 v23, v23, v6
	v_mul_f32_e32 v24, v24, v6
	v_mul_f32_e32 v25, v25, v6
	v_mul_f32_e32 v26, v26, v6
	v_mul_f32_e32 v27, v27, v6
	v_mul_f32_e32 v28, v28, v6
	v_mul_f32_e32 v29, v29, v6
	v_mul_f32_e32 v30, v30, v6
	v_mul_f32_e32 v31, v31, v6
	v_cvt_f32_i32_e32 v3, v3
	s_nop 0
	v_mul_f32_e32 v3, v3, v7
	ds_write_b128 v4, v[8:11]
	ds_write_b128 v4, v[12:15] offset:1024
	ds_write_b128 v4, v[16:19] offset:2048
	ds_write_b128 v4, v[20:23] offset:3072
	ds_write_b128 v4, v[24:27] offset:4096
	ds_write_b128 v4, v[28:31] offset:5120
	s_mov_b32 exec_lo, -1
	s_mov_b32 exec_hi, 0
	ds_write_b32 v5, v3 offset:55296
	s_mov_b64 exec, -1
	s_waitcnt lgkmcnt(0)
	s_barrier
	s_and_saveexec_b64 s[12:13], s[14:15]
	s_cbranch_execz .LBB0_572
	s_mov_b64 s[20:21], -1
	v_mov_b32_e32 v1, v152
	s_and_saveexec_b64 s[16:17], s[18:19]
	s_cbranch_execz .LBB0_569
	v_mov_b32_e32 v2, 0
	s_and_saveexec_b64 s[20:21], s[6:7]
	s_cbranch_execz .LBB0_565
	s_mov_b32 s42, 0
	s_mov_b64 s[46:47], 0
	v_mov_b32_e32 v0, v179
	v_mov_b32_e32 v1, v176
